# v29
# speedup vs baseline: 1.0023x; 1.0023x over previous
.LBB2_20:
	s_add_u32 s30, s28, 0xffc80080
	s_addc_u32 s31, s29, -1
	s_cmpk_eq_i32 s58, 0xdc
	s_cselect_b32 s35, s25, s31
	s_cselect_b32 s34, s24, s30
	s_cselect_b32 s31, s27, s57
	s_cselect_b32 s30, s26, s56
	s_add_i32 m0, s37, 0xc000
	ds_read_b128 a[0:3], v143
	ds_read_b128 a[4:7], v147
	ds_read_b128 a[8:11], v149
	ds_read_b128 a[12:15], v150
	ds_read_b128 a[16:19], v151
	ds_read_b128 a[20:23], v152
	ds_read_b128 a[24:27], v153
	ds_read_b128 a[28:31], v154
	ds_read_b128 a[32:35], v155
	ds_read_b128 a[36:39], v155 offset:2048
	ds_read_b128 a[40:43], v156
	ds_read_b128 a[44:47], v156 offset:2048
	ds_read_b128 a[48:51], v155 offset:4096
	ds_read_b128 a[52:55], v155 offset:6144
	ds_read_b128 a[56:59], v156 offset:4096
	ds_read_b128 a[60:63], v156 offset:6144
	global_load_lds_dwordx4 v134, s[28:29]
	s_add_i32 m0, s37, 0xe000
	s_nop 0
	global_load_lds_dwordx4 v132, s[28:29]
	s_waitcnt vmcnt(8)
	s_waitcnt lgkmcnt(0)
	s_barrier
	v_mfma_f32_16x16x32_f16 v[124:127], a[0:3], a[32:35], v[124:127]
	v_mfma_f32_16x16x32_f16 v[124:127], a[4:7], a[40:43], v[124:127]
	v_mfma_f32_16x16x32_f16 v[120:123], a[12:15], a[40:43], v[120:123]
	v_mfma_f32_16x16x32_f16 v[120:123], a[8:11], a[32:35], v[120:123]
	v_mfma_f32_16x16x32_f16 v[112:115], a[8:11], a[36:39], v[112:115]
	v_mfma_f32_16x16x32_f16 v[112:115], a[12:15], a[44:47], v[112:115]
	v_mfma_f32_16x16x32_f16 v[116:119], a[4:7], a[44:47], v[116:119]
	v_mfma_f32_16x16x32_f16 v[116:119], a[0:3], a[36:39], v[116:119]
	v_mfma_f32_16x16x32_f16 v[108:111], a[0:3], a[48:51], v[108:111]
	v_mfma_f32_16x16x32_f16 v[108:111], a[4:7], a[56:59], v[108:111]
	v_mfma_f32_16x16x32_f16 v[100:103], a[12:15], a[56:59], v[100:103]
	v_mfma_f32_16x16x32_f16 v[100:103], a[8:11], a[48:51], v[100:103]
	v_mfma_f32_16x16x32_f16 v[84:87], a[8:11], a[52:55], v[84:87]
	v_mfma_f32_16x16x32_f16 v[84:87], a[12:15], a[60:63], v[84:87]
	v_mfma_f32_16x16x32_f16 v[92:95], a[4:7], a[60:63], v[92:95]
	v_mfma_f32_16x16x32_f16 v[92:95], a[0:3], a[52:55], v[92:95]
	v_mfma_f32_16x16x32_f16 v[104:107], a[16:19], a[32:35], v[104:107]
	v_mfma_f32_16x16x32_f16 v[104:107], a[20:23], a[40:43], v[104:107]
	v_mfma_f32_16x16x32_f16 v[96:99], a[28:31], a[40:43], v[96:99]
	v_mfma_f32_16x16x32_f16 v[96:99], a[24:27], a[32:35], v[96:99]
	v_mfma_f32_16x16x32_f16 v[80:83], a[24:27], a[36:39], v[80:83]
	v_mfma_f32_16x16x32_f16 v[80:83], a[28:31], a[44:47], v[80:83]
	v_mfma_f32_16x16x32_f16 v[88:91], a[20:23], a[44:47], v[88:91]
	v_mfma_f32_16x16x32_f16 v[88:91], a[16:19], a[36:39], v[88:91]
	v_mfma_f32_16x16x32_f16 v[76:79], a[16:19], a[48:51], v[76:79]
	v_mfma_f32_16x16x32_f16 v[76:79], a[20:23], a[56:59], v[76:79]
	v_mfma_f32_16x16x32_f16 v[72:75], a[28:31], a[56:59], v[72:75]
	v_mfma_f32_16x16x32_f16 v[72:75], a[24:27], a[48:51], v[72:75]
	v_mfma_f32_16x16x32_f16 v[64:67], a[24:27], a[52:55], v[64:67]
	v_mfma_f32_16x16x32_f16 v[64:67], a[28:31], a[60:63], v[64:67]
	v_mfma_f32_16x16x32_f16 v[68:71], a[20:23], a[60:63], v[68:71]
	v_mfma_f32_16x16x32_f16 v[68:71], a[16:19], a[52:55], v[68:71]
	s_barrier
	s_add_i32 s59, s43, s36
	s_mov_b32 m0, s59
	ds_read_b128 a[32:35], v155 offset:16384
	ds_read_b128 a[36:39], v155 offset:18432
	ds_read_b128 a[40:43], v156 offset:16384
	ds_read_b128 a[44:47], v156 offset:18432
	ds_read_b128 a[48:51], v155 offset:20480
	ds_read_b128 a[52:55], v155 offset:22528
	ds_read_b128 a[56:59], v156 offset:20480
	ds_read_b128 a[60:63], v156 offset:22528
	global_load_lds_dwordx4 v128, s[30:31]
	s_add_i32 m0, s59, 0x2000
	s_add_u32 s60, s30, 0x380000
	s_addc_u32 s61, s31, 0
	s_add_i32 s59, s44, s36
	global_load_lds_dwordx4 v130, s[30:31]
	s_mov_b32 m0, s59
	s_add_u32 s62, s30, 0x80
	s_addc_u32 s63, s31, 0
	global_load_lds_dwordx4 v128, s[60:61]
	s_add_i32 m0, s59, 0x2000
	s_add_u32 s64, s34, 0x80
	s_addc_u32 s65, s35, 0
	global_load_lds_dwordx4 v130, s[60:61]
	s_mov_b32 m0, s37
	s_nop 0
	global_load_lds_dwordx4 v128, s[34:35]
	s_mov_b32 m0, s38
	s_nop 0
	global_load_lds_dwordx4 v130, s[34:35]
	s_waitcnt vmcnt(8)
	s_waitcnt lgkmcnt(0)
	s_barrier
	v_mfma_f32_16x16x32_f16 v[60:63], a[0:3], a[32:35], v[60:63]
	v_mfma_f32_16x16x32_f16 v[60:63], a[4:7], a[40:43], v[60:63]
	v_mfma_f32_16x16x32_f16 v[56:59], a[12:15], a[40:43], v[56:59]
	v_mfma_f32_16x16x32_f16 v[56:59], a[8:11], a[32:35], v[56:59]
	v_mfma_f32_16x16x32_f16 v[48:51], a[8:11], a[36:39], v[48:51]
	v_mfma_f32_16x16x32_f16 v[48:51], a[12:15], a[44:47], v[48:51]
	v_mfma_f32_16x16x32_f16 v[52:55], a[4:7], a[44:47], v[52:55]
	v_mfma_f32_16x16x32_f16 v[52:55], a[0:3], a[36:39], v[52:55]
	v_mfma_f32_16x16x32_f16 v[40:43], a[0:3], a[48:51], v[40:43]
	v_mfma_f32_16x16x32_f16 v[40:43], a[4:7], a[56:59], v[40:43]
	v_mfma_f32_16x16x32_f16 v[32:35], a[12:15], a[56:59], v[32:35]
	v_mfma_f32_16x16x32_f16 v[32:35], a[8:11], a[48:51], v[32:35]
	v_mfma_f32_16x16x32_f16 v[8:11], a[8:11], a[52:55], v[8:11]
	v_mfma_f32_16x16x32_f16 v[8:11], a[12:15], a[60:63], v[8:11]
	v_mfma_f32_16x16x32_f16 v[12:15], a[4:7], a[60:63], v[12:15]
	v_mfma_f32_16x16x32_f16 v[12:15], a[0:3], a[52:55], v[12:15]
	v_mfma_f32_16x16x32_f16 v[44:47], a[16:19], a[32:35], v[44:47]
	v_mfma_f32_16x16x32_f16 v[44:47], a[20:23], a[40:43], v[44:47]
	v_mfma_f32_16x16x32_f16 v[36:39], a[28:31], a[40:43], v[36:39]
	v_mfma_f32_16x16x32_f16 v[36:39], a[24:27], a[32:35], v[36:39]
	v_mfma_f32_16x16x32_f16 v[24:27], a[24:27], a[36:39], v[24:27]
	v_mfma_f32_16x16x32_f16 v[24:27], a[28:31], a[44:47], v[24:27]
	v_mfma_f32_16x16x32_f16 v[28:31], a[20:23], a[44:47], v[28:31]
	v_mfma_f32_16x16x32_f16 v[28:31], a[16:19], a[36:39], v[28:31]
	v_mfma_f32_16x16x32_f16 v[20:23], a[16:19], a[48:51], v[20:23]
	v_mfma_f32_16x16x32_f16 v[20:23], a[20:23], a[56:59], v[20:23]
	v_mfma_f32_16x16x32_f16 v[16:19], a[28:31], a[56:59], v[16:19]
	v_mfma_f32_16x16x32_f16 v[16:19], a[24:27], a[48:51], v[16:19]
	v_mfma_f32_16x16x32_f16 v[0:3], a[24:27], a[52:55], v[0:3]
	v_mfma_f32_16x16x32_f16 v[0:3], a[28:31], a[60:63], v[0:3]
	v_mfma_f32_16x16x32_f16 v[4:7], a[20:23], a[60:63], v[4:7]
	v_mfma_f32_16x16x32_f16 v[4:7], a[16:19], a[52:55], v[4:7]
	s_barrier
	s_add_u32 s34, s34, 0x380000
	s_addc_u32 s35, s35, 0
	s_mov_b32 m0, s39
	ds_read_b128 a[0:3], v157
	ds_read_b128 a[4:7], v158
	ds_read_b128 a[8:11], v159
	ds_read_b128 a[12:15], v160
	ds_read_b128 a[16:19], v161
	ds_read_b128 a[20:23], v162
	ds_read_b128 a[24:27], v163
	ds_read_b128 a[28:31], v164
	ds_read_b128 a[32:35], v155 offset:32768
	ds_read_b128 a[36:39], v155 offset:34816
	ds_read_b128 a[40:43], v156 offset:32768
	ds_read_b128 a[44:47], v156 offset:34816
	ds_read_b128 a[48:51], v155 offset:36864
	ds_read_b128 a[52:55], v155 offset:38912
	ds_read_b128 a[56:59], v156 offset:36864
	ds_read_b128 a[60:63], v156 offset:38912
	global_load_lds_dwordx4 v128, s[34:35]
	s_mov_b32 m0, s40
	s_nop 0
	global_load_lds_dwordx4 v130, s[34:35]
	s_waitcnt vmcnt(8)
	s_waitcnt lgkmcnt(0)
	s_barrier
	v_mfma_f32_16x16x32_f16 v[124:127], a[0:3], a[32:35], v[124:127]
	v_mfma_f32_16x16x32_f16 v[124:127], a[4:7], a[40:43], v[124:127]
	v_mfma_f32_16x16x32_f16 v[120:123], a[12:15], a[40:43], v[120:123]
	v_mfma_f32_16x16x32_f16 v[120:123], a[8:11], a[32:35], v[120:123]
	v_mfma_f32_16x16x32_f16 v[112:115], a[8:11], a[36:39], v[112:115]
	v_mfma_f32_16x16x32_f16 v[112:115], a[12:15], a[44:47], v[112:115]
	v_mfma_f32_16x16x32_f16 v[116:119], a[4:7], a[44:47], v[116:119]
	v_mfma_f32_16x16x32_f16 v[116:119], a[0:3], a[36:39], v[116:119]
	v_mfma_f32_16x16x32_f16 v[108:111], a[0:3], a[48:51], v[108:111]
	v_mfma_f32_16x16x32_f16 v[108:111], a[4:7], a[56:59], v[108:111]
	v_mfma_f32_16x16x32_f16 v[100:103], a[12:15], a[56:59], v[100:103]
	v_mfma_f32_16x16x32_f16 v[100:103], a[8:11], a[48:51], v[100:103]
	v_mfma_f32_16x16x32_f16 v[84:87], a[8:11], a[52:55], v[84:87]
	v_mfma_f32_16x16x32_f16 v[84:87], a[12:15], a[60:63], v[84:87]
	v_mfma_f32_16x16x32_f16 v[92:95], a[4:7], a[60:63], v[92:95]
	v_mfma_f32_16x16x32_f16 v[92:95], a[0:3], a[52:55], v[92:95]
	v_mfma_f32_16x16x32_f16 v[104:107], a[16:19], a[32:35], v[104:107]
	v_mfma_f32_16x16x32_f16 v[104:107], a[20:23], a[40:43], v[104:107]
	v_mfma_f32_16x16x32_f16 v[96:99], a[28:31], a[40:43], v[96:99]
	v_mfma_f32_16x16x32_f16 v[96:99], a[24:27], a[32:35], v[96:99]
	v_mfma_f32_16x16x32_f16 v[80:83], a[24:27], a[36:39], v[80:83]
	v_mfma_f32_16x16x32_f16 v[80:83], a[28:31], a[44:47], v[80:83]
	v_mfma_f32_16x16x32_f16 v[88:91], a[20:23], a[44:47], v[88:91]
	v_mfma_f32_16x16x32_f16 v[88:91], a[16:19], a[36:39], v[88:91]
	v_mfma_f32_16x16x32_f16 v[76:79], a[16:19], a[48:51], v[76:79]
	v_mfma_f32_16x16x32_f16 v[76:79], a[20:23], a[56:59], v[76:79]
	v_mfma_f32_16x16x32_f16 v[72:75], a[28:31], a[56:59], v[72:75]
	v_mfma_f32_16x16x32_f16 v[72:75], a[24:27], a[48:51], v[72:75]
	v_mfma_f32_16x16x32_f16 v[64:67], a[24:27], a[52:55], v[64:67]
	v_mfma_f32_16x16x32_f16 v[64:67], a[28:31], a[60:63], v[64:67]
	v_mfma_f32_16x16x32_f16 v[68:71], a[20:23], a[60:63], v[68:71]
	v_mfma_f32_16x16x32_f16 v[68:71], a[16:19], a[52:55], v[68:71]
	s_barrier
	s_add_i32 s34, s46, s36
	s_mov_b32 m0, s34
	ds_read_b128 a[32:35], v155 offset:49152
	ds_read_b128 a[36:39], v155 offset:51200
	ds_read_b128 a[40:43], v156 offset:49152
	ds_read_b128 a[44:47], v156 offset:51200
	ds_read_b128 a[48:51], v155 offset:53248
	ds_read_b128 a[52:55], v155 offset:55296
	ds_read_b128 a[56:59], v156 offset:53248
	ds_read_b128 a[60:63], v156 offset:55296
	global_load_lds_dwordx4 v128, s[62:63]
	s_add_i32 m0, s34, 0x2000
	s_add_u32 s30, s30, 0x380080
	s_addc_u32 s31, s31, 0
	s_add_i32 s34, s47, s36
	global_load_lds_dwordx4 v130, s[62:63]
	s_mov_b32 m0, s34
	s_nop 0
	global_load_lds_dwordx4 v128, s[30:31]
	s_add_i32 m0, s34, 0x2000
	s_nop 0
	global_load_lds_dwordx4 v130, s[30:31]
	s_mov_b32 m0, s41
	s_nop 0
	global_load_lds_dwordx4 v128, s[64:65]
	s_mov_b32 m0, s42
	s_nop 0
	global_load_lds_dwordx4 v130, s[64:65]
	s_waitcnt vmcnt(8)
	s_waitcnt lgkmcnt(0)
	s_barrier
	v_mfma_f32_16x16x32_f16 v[60:63], a[0:3], a[32:35], v[60:63]
	v_mfma_f32_16x16x32_f16 v[60:63], a[4:7], a[40:43], v[60:63]
	v_mfma_f32_16x16x32_f16 v[56:59], a[12:15], a[40:43], v[56:59]
	v_mfma_f32_16x16x32_f16 v[56:59], a[8:11], a[32:35], v[56:59]
	v_mfma_f32_16x16x32_f16 v[48:51], a[8:11], a[36:39], v[48:51]
	v_mfma_f32_16x16x32_f16 v[48:51], a[12:15], a[44:47], v[48:51]
	v_mfma_f32_16x16x32_f16 v[52:55], a[4:7], a[44:47], v[52:55]
	v_mfma_f32_16x16x32_f16 v[52:55], a[0:3], a[36:39], v[52:55]
	v_mfma_f32_16x16x32_f16 v[40:43], a[0:3], a[48:51], v[40:43]
	v_mfma_f32_16x16x32_f16 v[40:43], a[4:7], a[56:59], v[40:43]
	v_mfma_f32_16x16x32_f16 v[32:35], a[12:15], a[56:59], v[32:35]
	v_mfma_f32_16x16x32_f16 v[32:35], a[8:11], a[48:51], v[32:35]
	v_mfma_f32_16x16x32_f16 v[8:11], a[8:11], a[52:55], v[8:11]
	v_mfma_f32_16x16x32_f16 v[8:11], a[12:15], a[60:63], v[8:11]
	v_mfma_f32_16x16x32_f16 v[12:15], a[4:7], a[60:63], v[12:15]
	v_mfma_f32_16x16x32_f16 v[12:15], a[0:3], a[52:55], v[12:15]
	v_mfma_f32_16x16x32_f16 v[44:47], a[16:19], a[32:35], v[44:47]
	v_mfma_f32_16x16x32_f16 v[44:47], a[20:23], a[40:43], v[44:47]
	v_mfma_f32_16x16x32_f16 v[36:39], a[28:31], a[40:43], v[36:39]
	v_mfma_f32_16x16x32_f16 v[36:39], a[24:27], a[32:35], v[36:39]
	v_mfma_f32_16x16x32_f16 v[24:27], a[24:27], a[36:39], v[24:27]
	v_mfma_f32_16x16x32_f16 v[24:27], a[28:31], a[44:47], v[24:27]
	v_mfma_f32_16x16x32_f16 v[28:31], a[20:23], a[44:47], v[28:31]
	v_mfma_f32_16x16x32_f16 v[28:31], a[16:19], a[36:39], v[28:31]
	v_mfma_f32_16x16x32_f16 v[20:23], a[16:19], a[48:51], v[20:23]
	v_mfma_f32_16x16x32_f16 v[20:23], a[20:23], a[56:59], v[20:23]
	v_mfma_f32_16x16x32_f16 v[16:19], a[28:31], a[56:59], v[16:19]
	v_mfma_f32_16x16x32_f16 v[16:19], a[24:27], a[48:51], v[16:19]
	v_mfma_f32_16x16x32_f16 v[0:3], a[24:27], a[52:55], v[0:3]
	v_mfma_f32_16x16x32_f16 v[0:3], a[28:31], a[60:63], v[0:3]
	v_mfma_f32_16x16x32_f16 v[4:7], a[20:23], a[60:63], v[4:7]
	v_mfma_f32_16x16x32_f16 v[4:7], a[16:19], a[52:55], v[4:7]
	s_barrier
	s_add_i32 s58, s58, 2
	s_add_u32 s56, s56, 0x100
	s_addc_u32 s57, s57, 0
	s_add_u32 s28, s28, 0x100
	s_addc_u32 s29, s29, 0
	s_cmpk_gt_u32 s58, 0xdd
	s_cbranch_scc0 .LBB2_20
	v_lshl_add_u32 v144, s55, 8, v137
	v_ashrrev_i32_e32 v145, 31, v144
	v_lshl_add_u64 v[138:139], v[144:145], 2, s[10:11]
	global_load_dword v136, v[138:139], off
	global_load_dword v140, v[138:139], off offset:64
	global_load_dword v142, v[138:139], off offset:128
	global_load_dword v146, v[138:139], off offset:192
	global_load_dword v148, v[138:139], off offset:512
	global_load_dword v174, v[138:139], off offset:576
	global_load_dword v176, v[138:139], off offset:640
	s_nop 0
	global_load_dword v138, v[138:139], off offset:704
	v_lshl_or_b32 v166, s54, 8, v141
	v_ashrrev_i32_e32 v167, 31, v166
	v_or_b32_e32 v168, 16, v144
	v_or_b32_e32 v170, 32, v144
	v_or_b32_e32 v172, 48, v144
	v_lshl_add_u64 v[166:167], v[166:167], 2, s[8:9]
	v_lshlrev_b64 v[144:145], 14, v[144:145]
	v_ashrrev_i32_e32 v169, 31, v168
	v_ashrrev_i32_e32 v171, 31, v170
	v_ashrrev_i32_e32 v173, 31, v172
	v_lshl_add_u64 v[144:145], v[166:167], 0, v[144:145]
	v_lshlrev_b64 v[168:169], 14, v[168:169]
	v_lshlrev_b64 v[170:171], 14, v[170:171]
	v_lshlrev_b64 v[172:173], 14, v[172:173]
	v_add_co_u32_e32 v178, vcc, s48, v144
	v_lshl_add_u64 v[168:169], v[166:167], 0, v[168:169]
	v_lshl_add_u64 v[170:171], v[166:167], 0, v[170:171]
	v_lshl_add_u64 v[166:167], v[166:167], 0, v[172:173]
	v_lshl_add_u64 v[172:173], v[144:145], 0, s[16:17]
	v_addc_co_u32_e32 v179, vcc, 0, v145, vcc
	s_mov_b32 s55, s45
	s_mov_b32 s54, s53
	s_mov_b64 s[28:29], s[26:27]
	s_mov_b64 s[30:31], s[24:25]
	s_waitcnt vmcnt(0)
	v_pk_mul_f32 v[126:127], v[136:137], v[126:127] op_sel_hi:[0,1]
	v_pk_mul_f32 v[124:125], v[136:137], v[124:125] op_sel_hi:[0,1]
	v_pk_mul_f32 v[122:123], v[136:137], v[122:123] op_sel_hi:[0,1]
	v_pk_mul_f32 v[120:121], v[136:137], v[120:121] op_sel_hi:[0,1]
	v_pk_mul_f32 v[46:47], v[148:149], v[46:47] op_sel_hi:[0,1]
	v_pk_mul_f32 v[44:45], v[148:149], v[44:45] op_sel_hi:[0,1]
	v_pk_mul_f32 v[106:107], v[136:137], v[106:107] op_sel_hi:[0,1]
	v_pk_mul_f32 v[104:105], v[136:137], v[104:105] op_sel_hi:[0,1]
	v_pk_mul_f32 v[98:99], v[136:137], v[98:99] op_sel_hi:[0,1]
	v_pk_mul_f32 v[96:97], v[136:137], v[96:97] op_sel_hi:[0,1]
	v_pk_mul_f32 v[118:119], v[140:141], v[118:119] op_sel_hi:[0,1]
	v_pk_mul_f32 v[116:117], v[140:141], v[116:117] op_sel_hi:[0,1]
	v_pk_mul_f32 v[114:115], v[140:141], v[114:115] op_sel_hi:[0,1]
	v_pk_mul_f32 v[112:113], v[140:141], v[112:113] op_sel_hi:[0,1]
	v_pk_mul_f32 v[90:91], v[140:141], v[90:91] op_sel_hi:[0,1]
	v_pk_mul_f32 v[88:89], v[140:141], v[88:89] op_sel_hi:[0,1]
	v_pk_mul_f32 v[82:83], v[140:141], v[82:83] op_sel_hi:[0,1]
	v_pk_mul_f32 v[80:81], v[140:141], v[80:81] op_sel_hi:[0,1]
	v_pk_mul_f32 v[110:111], v[142:143], v[110:111] op_sel_hi:[0,1]
	v_pk_mul_f32 v[108:109], v[142:143], v[108:109] op_sel_hi:[0,1]
	v_pk_mul_f32 v[102:103], v[142:143], v[102:103] op_sel_hi:[0,1]
	v_pk_mul_f32 v[100:101], v[142:143], v[100:101] op_sel_hi:[0,1]
	v_pk_mul_f32 v[78:79], v[142:143], v[78:79] op_sel_hi:[0,1]
	v_pk_mul_f32 v[76:77], v[142:143], v[76:77] op_sel_hi:[0,1]
	v_pk_mul_f32 v[74:75], v[142:143], v[74:75] op_sel_hi:[0,1]
	v_pk_mul_f32 v[72:73], v[142:143], v[72:73] op_sel_hi:[0,1]
	v_pk_mul_f32 v[94:95], v[146:147], v[94:95] op_sel_hi:[0,1]
	v_pk_mul_f32 v[92:93], v[146:147], v[92:93] op_sel_hi:[0,1]
	v_pk_mul_f32 v[86:87], v[146:147], v[86:87] op_sel_hi:[0,1]
	v_pk_mul_f32 v[84:85], v[146:147], v[84:85] op_sel_hi:[0,1]
	v_pk_mul_f32 v[70:71], v[146:147], v[70:71] op_sel_hi:[0,1]
	v_pk_mul_f32 v[68:69], v[146:147], v[68:69] op_sel_hi:[0,1]
	v_pk_mul_f32 v[66:67], v[146:147], v[66:67] op_sel_hi:[0,1]
	v_pk_mul_f32 v[64:65], v[146:147], v[64:65] op_sel_hi:[0,1]
	v_pk_mul_f32 v[62:63], v[148:149], v[62:63] op_sel_hi:[0,1]
	v_pk_mul_f32 v[60:61], v[148:149], v[60:61] op_sel_hi:[0,1]
	global_store_dwordx4 v[144:145], v[124:127], off
	global_store_dwordx4 v[144:145], v[120:123], off offset:64
	global_store_dwordx4 v[144:145], v[104:107], off offset:512
	global_store_dwordx4 v[144:145], v[96:99], off offset:576
	global_store_dwordx4 v[168:169], v[116:119], off
	global_store_dwordx4 v[168:169], v[112:115], off offset:64
	global_store_dwordx4 v[168:169], v[88:91], off offset:512
	global_store_dwordx4 v[168:169], v[80:83], off offset:576
	global_store_dwordx4 v[170:171], v[108:111], off
	global_store_dwordx4 v[170:171], v[100:103], off offset:64
	global_store_dwordx4 v[170:171], v[76:79], off offset:512
	global_store_dwordx4 v[170:171], v[72:75], off offset:576
	global_store_dwordx4 v[166:167], v[92:95], off
	global_store_dwordx4 v[166:167], v[84:87], off offset:64
	global_store_dwordx4 v[166:167], v[68:71], off offset:512
	global_store_dwordx4 v[166:167], v[64:67], off offset:576
	global_store_dwordx4 v[178:179], v[60:63], off
	global_store_dwordx4 v[172:173], v[44:47], off offset:512
	v_pk_mul_f32 v[30:31], v[174:175], v[30:31] op_sel_hi:[0,1]
	v_pk_mul_f32 v[28:29], v[174:175], v[28:29] op_sel_hi:[0,1]
	v_add_co_u32_e32 v46, vcc, s49, v144
	v_lshl_add_u64 v[44:45], v[144:145], 0, s[18:19]
	s_nop 0
	v_addc_co_u32_e32 v47, vcc, 0, v145, vcc
	global_store_dwordx4 v[44:45], v[28:31], off offset:512
	v_pk_mul_f32 v[18:19], v[176:177], v[18:19] op_sel_hi:[0,1]
	v_pk_mul_f32 v[16:17], v[176:177], v[16:17] op_sel_hi:[0,1]
	v_add_co_u32_e32 v30, vcc, s50, v144
	v_lshl_add_u64 v[28:29], v[144:145], 0, s[20:21]
	s_nop 0
	v_addc_co_u32_e32 v31, vcc, 0, v145, vcc
	v_pk_mul_f32 v[38:39], v[148:149], v[38:39] op_sel_hi:[0,1]
	v_pk_mul_f32 v[36:37], v[148:149], v[36:37] op_sel_hi:[0,1]
	v_pk_mul_f32 v[26:27], v[174:175], v[26:27] op_sel_hi:[0,1]
	v_pk_mul_f32 v[24:25], v[174:175], v[24:25] op_sel_hi:[0,1]
	global_store_dwordx4 v[28:29], v[16:19], off offset:576
	global_store_dwordx4 v[172:173], v[36:39], off offset:576
	global_store_dwordx4 v[44:45], v[24:27], off offset:576
	v_add_co_u32_e32 v18, vcc, s51, v144
	v_pk_mul_f32 v[38:39], v[174:175], v[54:55] op_sel_hi:[0,1]
	v_pk_mul_f32 v[36:37], v[174:175], v[52:53] op_sel_hi:[0,1]
	v_pk_mul_f32 v[26:27], v[176:177], v[42:43] op_sel_hi:[0,1]
	v_pk_mul_f32 v[24:25], v[176:177], v[40:41] op_sel_hi:[0,1]
	v_addc_co_u32_e32 v19, vcc, 0, v145, vcc
	v_pk_mul_f32 v[58:59], v[148:149], v[58:59] op_sel_hi:[0,1]
	v_pk_mul_f32 v[56:57], v[148:149], v[56:57] op_sel_hi:[0,1]
	global_store_dwordx4 v[46:47], v[36:39], off
	global_store_dwordx4 v[30:31], v[24:27], off
	v_pk_mul_f32 v[22:23], v[176:177], v[22:23] op_sel_hi:[0,1]
	v_pk_mul_f32 v[38:39], v[174:175], v[50:51] op_sel_hi:[0,1]
	v_pk_mul_f32 v[36:37], v[174:175], v[48:49] op_sel_hi:[0,1]
	v_pk_mul_f32 v[26:27], v[176:177], v[34:35] op_sel_hi:[0,1]
	v_pk_mul_f32 v[24:25], v[176:177], v[32:33] op_sel_hi:[0,1]
	v_pk_mul_f32 v[20:21], v[176:177], v[20:21] op_sel_hi:[0,1]
	v_lshl_add_u64 v[16:17], v[144:145], 0, s[22:23]
	v_pk_mul_f32 v[14:15], v[138:139], v[14:15] op_sel_hi:[0,1]
	v_pk_mul_f32 v[12:13], v[138:139], v[12:13] op_sel_hi:[0,1]
	v_pk_mul_f32 v[10:11], v[138:139], v[10:11] op_sel_hi:[0,1]
	v_pk_mul_f32 v[8:9], v[138:139], v[8:9] op_sel_hi:[0,1]
	v_pk_mul_f32 v[6:7], v[138:139], v[6:7] op_sel_hi:[0,1]
	v_pk_mul_f32 v[4:5], v[138:139], v[4:5] op_sel_hi:[0,1]
	v_pk_mul_f32 v[2:3], v[138:139], v[2:3] op_sel_hi:[0,1]
	v_pk_mul_f32 v[0:1], v[138:139], v[0:1] op_sel_hi:[0,1]
	s_mov_b64 vcc, s[0:1]
	global_store_dwordx4 v[172:173], v[56:59], off offset:64
	global_store_dwordx4 v[44:45], v[36:39], off offset:64
	global_store_dwordx4 v[28:29], v[24:27], off offset:64
	global_store_dwordx4 v[28:29], v[20:23], off offset:512
	global_store_dwordx4 v[18:19], v[12:15], off
	global_store_dwordx4 v[16:17], v[8:11], off offset:64
	global_store_dwordx4 v[16:17], v[4:7], off offset:512
	global_store_dwordx4 v[16:17], v[0:3], off offset:576
	s_cbranch_vccz .LBB2_8
	s_waitcnt vmcnt(0)
	s_cmpk_gt_u32 s33, 0xff
	s_cbranch_scc1 .LBB2_24
	s_barrier

	.amdhsa_kernel _Z12gemm_persistILi1ELi14336ELi32ELi16EEvPKDF16_S1_PvPKfS4_S4_S4_PDF16_S5_iii
		.amdhsa_group_segment_fixed_size 0
		.amdhsa_private_segment_fixed_size 0
		.amdhsa_kernarg_size 344
		.amdhsa_user_sgpr_count 2
		.amdhsa_user_sgpr_dispatch_ptr 0
		.amdhsa_user_sgpr_queue_ptr 0
		.amdhsa_user_sgpr_kernarg_segment_ptr 1
		.amdhsa_user_sgpr_dispatch_id 0
		.amdhsa_user_sgpr_kernarg_preload_length 0
		.amdhsa_user_sgpr_kernarg_preload_offset 0
		.amdhsa_user_sgpr_private_segment_size 0
		.amdhsa_uses_dynamic_stack 0
		.amdhsa_enable_private_segment 0
		.amdhsa_system_sgpr_workgroup_id_x 1
		.amdhsa_system_sgpr_workgroup_id_y 0
		.amdhsa_system_sgpr_workgroup_id_z 0
		.amdhsa_system_sgpr_workgroup_info 0
		.amdhsa_system_vgpr_workitem_id 0
		.amdhsa_next_free_vgpr 244
		.amdhsa_next_free_sgpr 66
		.amdhsa_accum_offset 180
		.amdhsa_reserve_vcc 1
		.amdhsa_float_round_mode_32 0
		.amdhsa_float_round_mode_16_64 0
		.amdhsa_float_denorm_mode_32 3
		.amdhsa_float_denorm_mode_16_64 3
		.amdhsa_dx10_clamp 1
		.amdhsa_ieee_mode 1
		.amdhsa_fp16_overflow 0
		.amdhsa_tg_split 0
		.amdhsa_exception_fp_ieee_invalid_op 0
		.amdhsa_exception_fp_denorm_src 0
		.amdhsa_exception_fp_ieee_div_zero 0
		.amdhsa_exception_fp_ieee_overflow 0
		.amdhsa_exception_fp_ieee_underflow 0
		.amdhsa_exception_fp_ieee_inexact 0
		.amdhsa_exception_int_div_zero 0
	.end_amdhsa_kernel

amdhsa.kernels:
  - .agpr_count:     4
    .args:
      - .actual_access:  read_only
        .address_space:  global
        .offset:         0
        .size:           8
        .value_kind:     global_buffer
      - .actual_access:  read_only
        .address_space:  global
        .offset:         8
        .size:           8
        .value_kind:     global_buffer
      - .actual_access:  read_only
        .address_space:  global
        .offset:         16
        .size:           8
        .value_kind:     global_buffer
      - .actual_access:  read_only
        .address_space:  global
        .offset:         24
        .size:           8
        .value_kind:     global_buffer
      - .actual_access:  write_only
        .address_space:  global
        .offset:         32
        .size:           8
        .value_kind:     global_buffer
      - .actual_access:  write_only
        .address_space:  global
        .offset:         40
        .size:           8
        .value_kind:     global_buffer
      - .actual_access:  write_only
        .address_space:  global
        .offset:         48
        .size:           8
        .value_kind:     global_buffer
    .group_segment_fixed_size: 4352
    .kernarg_segment_align: 8
    .kernarg_segment_size: 56
    .language:       OpenCL C
    .language_version:
      - 2
      - 0
    .max_flat_workgroup_size: 256
    .name:           _Z11prep_kernelPKfS0_S0_S0_PDF16_PfS1_
    .private_segment_fixed_size: 0
    .sgpr_count:     26
    .sgpr_spill_count: 0
    .symbol:         _Z11prep_kernelPKfS0_S0_S0_PDF16_PfS1_.kd
    .uniform_work_group_size: 1
    .uses_dynamic_stack: false
    .vgpr_count:     56
    .vgpr_spill_count: 0
    .wavefront_size: 64
  - .agpr_count:     0
    .args:
      - .address_space:  global
        .offset:         0
        .size:           8
        .value_kind:     global_buffer
      - .address_space:  global
        .offset:         8
        .size:           8
        .value_kind:     global_buffer
      - .actual_access:  write_only
        .address_space:  global
        .offset:         16
        .size:           8
        .value_kind:     global_buffer
      - .actual_access:  read_only
        .address_space:  global
        .offset:         24
        .size:           8
        .value_kind:     global_buffer
      - .address_space:  global
        .offset:         32
        .size:           8
        .value_kind:     global_buffer
      - .address_space:  global
        .offset:         40
        .size:           8
        .value_kind:     global_buffer
      - .address_space:  global
        .offset:         48
        .size:           8
        .value_kind:     global_buffer
      - .actual_access:  write_only
        .address_space:  global
        .offset:         56
        .size:           8
        .value_kind:     global_buffer
      - .actual_access:  write_only
        .address_space:  global
        .offset:         64
        .size:           8
        .value_kind:     global_buffer
      - .offset:         72
        .size:           4
        .value_kind:     by_value
      - .offset:         76
        .size:           4
        .value_kind:     by_value
      - .offset:         80
        .size:           4
        .value_kind:     by_value
      - .offset:         88
        .size:           4
        .value_kind:     hidden_block_count_x
      - .offset:         92
        .size:           4
        .value_kind:     hidden_block_count_y
      - .offset:         96
        .size:           4
        .value_kind:     hidden_block_count_z
      - .offset:         100
        .size:           2
        .value_kind:     hidden_group_size_x
      - .offset:         102
        .size:           2
        .value_kind:     hidden_group_size_y
      - .offset:         104
        .size:           2
        .value_kind:     hidden_group_size_z
      - .offset:         106
        .size:           2
        .value_kind:     hidden_remainder_x
      - .offset:         108
        .size:           2
        .value_kind:     hidden_remainder_y
      - .offset:         110
        .size:           2
        .value_kind:     hidden_remainder_z
      - .offset:         128
        .size:           8
        .value_kind:     hidden_global_offset_x
      - .offset:         136
        .size:           8
        .value_kind:     hidden_global_offset_y
      - .offset:         144
        .size:           8
        .value_kind:     hidden_global_offset_z
      - .offset:         152
        .size:           2
        .value_kind:     hidden_grid_dims
      - .offset:         208
        .size:           4
        .value_kind:     hidden_dynamic_lds_size
    .group_segment_fixed_size: 0
    .kernarg_segment_align: 8
    .kernarg_segment_size: 344
    .language:       OpenCL C
    .language_version:
      - 2
      - 0
    .max_flat_workgroup_size: 512
    .name:           _Z12gemm_persistILi0ELi4096ELi32ELi112EEvPKDF16_S1_PvPKfS4_S4_S4_PDF16_S5_iii
    .private_segment_fixed_size: 0
    .sgpr_count:     102
    .sgpr_spill_count: 0
    .symbol:         _Z12gemm_persistILi0ELi4096ELi32ELi112EEvPKDF16_S1_PvPKfS4_S4_S4_PDF16_S5_iii.kd
    .uniform_work_group_size: 1
    .uses_dynamic_stack: false
    .vgpr_count:     232
    .vgpr_spill_count: 0
    .wavefront_size: 64
  - .agpr_count:     64
    .args:
      - .address_space:  global
        .offset:         0
        .size:           8
        .value_kind:     global_buffer
      - .address_space:  global
        .offset:         8
        .size:           8
        .value_kind:     global_buffer
      - .actual_access:  write_only
        .address_space:  global
        .offset:         16
        .size:           8
        .value_kind:     global_buffer
      - .actual_access:  read_only
        .address_space:  global
        .offset:         24
        .size:           8
        .value_kind:     global_buffer
      - .actual_access:  read_only
        .address_space:  global
        .offset:         32
        .size:           8
        .value_kind:     global_buffer
      - .actual_access:  read_only
        .address_space:  global
        .offset:         40
        .size:           8
        .value_kind:     global_buffer
      - .actual_access:  read_only
        .address_space:  global
        .offset:         48
        .size:           8
        .value_kind:     global_buffer
      - .actual_access:  read_only
        .address_space:  global
        .offset:         56
        .size:           8
        .value_kind:     global_buffer
      - .actual_access:  read_only
        .address_space:  global
        .offset:         64
        .size:           8
        .value_kind:     global_buffer
      - .offset:         72
        .size:           4
        .value_kind:     by_value
      - .offset:         76
        .size:           4
        .value_kind:     by_value
      - .offset:         80
        .size:           4
        .value_kind:     by_value
      - .offset:         88
        .size:           4
        .value_kind:     hidden_block_count_x
      - .offset:         92
        .size:           4
        .value_kind:     hidden_block_count_y
      - .offset:         96
        .size:           4
        .value_kind:     hidden_block_count_z
      - .offset:         100
        .size:           2
        .value_kind:     hidden_group_size_x
      - .offset:         102
        .size:           2
        .value_kind:     hidden_group_size_y
      - .offset:         104
        .size:           2
        .value_kind:     hidden_group_size_z
      - .offset:         106
        .size:           2
        .value_kind:     hidden_remainder_x
      - .offset:         108
        .size:           2
        .value_kind:     hidden_remainder_y
      - .offset:         110
        .size:           2
        .value_kind:     hidden_remainder_z
      - .offset:         128
        .size:           8
        .value_kind:     hidden_global_offset_x
      - .offset:         136
        .size:           8
        .value_kind:     hidden_global_offset_y
      - .offset:         144
        .size:           8
        .value_kind:     hidden_global_offset_z
      - .offset:         152
        .size:           2
        .value_kind:     hidden_grid_dims
      - .offset:         208
        .size:           4
        .value_kind:     hidden_dynamic_lds_size
    .group_segment_fixed_size: 0
    .kernarg_segment_align: 8
    .kernarg_segment_size: 344
    .language:       OpenCL C
    .language_version:
      - 2
      - 0
    .max_flat_workgroup_size: 512
    .name:           _Z12gemm_persistILi1ELi14336ELi32ELi16EEvPKDF16_S1_PvPKfS4_S4_S4_PDF16_S5_iii
    .private_segment_fixed_size: 0
    .sgpr_count:     72
    .sgpr_spill_count: 0
    .symbol:         _Z12gemm_persistILi1ELi14336ELi32ELi16EEvPKDF16_S1_PvPKfS4_S4_S4_PDF16_S5_iii.kd
    .uniform_work_group_size: 1
    .uses_dynamic_stack: false
    .vgpr_count:     244
    .vgpr_spill_count: 0
    .wavefront_size: 64
